# speedup vs baseline: 1.0051x; 1.0005x over previous
.Lmk_p72:
	v_mov_b64_e32 v[130:131], 0
	v_mov_b64_e32 v[132:133], 0
	v_mov_b64_e32 v[134:135], 0
	v_mov_b64_e32 v[136:137], 0
	v_mov_b64_e32 v[138:139], 0
	v_mov_b64_e32 v[140:141], 0
	v_mov_b64_e32 v[142:143], 0
	v_mov_b64_e32 v[144:145], 0
	v_and_b32_e32 v200, 1, v114
	v_cmp_eq_u32_e32 vcc, 1, v200
	s_nop 1
	v_cndmask_b32_e32 v124, v124, v174, vcc
	v_mov_b64_e32 v[168:169], s[12:13]
	v_mov_b64_e32 v[170:171], s[12:13]
	v_xor_b32_e32 v117, 64, v122
	s_mov_b32 s30, s85
	s_lshl_b32 s6, s43, 6
	s_sub_i32 s83, s44, s6
	s_lshl_b32 s6, s43, 8
	s_add_i32 s82, s78, s6
	s_mov_b32 s66, s41
	s_branch .LBB2_62
